# stack + GEMM unit transitions: accumulator zeroing with v_mov_b64 pairs, gridDim kept in an SGPR instead of an s_load per unit
# speedup vs baseline: 1.0450x; 1.0028x over previous
.LBB0_5:
	s_or_b64 exec, exec, s[0:1]
	v_readlane_b32 s2, v254, 1
	s_lshr_b32 s46, s24, 6
	v_readlane_b32 s3, v254, 2
	v_writelane_b32 v254, s6, 14
	s_lshl_b32 s0, s6, 3
	v_writelane_b32 v254, s0, 15
	s_add_i32 s84, s46, s0
	s_load_dword s0, s[2:3], 0xb8
	s_load_dwordx2 s[4:5], s[2:3], 0xb0
	s_load_dwordx4 s[88:91], s[2:3], 0x0
	v_and_b32_e32 v236, 63, v0
	s_waitcnt lgkmcnt(0)
	s_mov_b32 s99, s0
	s_lshl_b32 s66, s0, 3
	s_cmp_lt_i32 s4, 1
	s_cselect_b64 s[0:1], -1, 0
	v_writelane_b32 v254, s4, 16
	s_cmp_gt_i32 s5, 0
	s_cselect_b64 s[2:3], -1, 0
	s_and_b64 s[8:9], s[0:1], s[2:3]
	v_writelane_b32 v254, s5, 17
	s_andn2_b64 vcc, exec, s[8:9]
	s_cbranch_vccnz .LBB0_96
	s_mul_i32 s0, s46, 0x4200
	s_add_i32 s14, s0, 0
	v_readlane_b32 s0, v254, 1
	v_readlane_b32 s1, v254, 2
	s_load_dwordx2 s[4:5], s[0:1], 0x10
	s_add_u32 s2, s86, 0x400000
	s_addc_u32 s3, s87, 0
	s_cmpk_gt_i32 s84, 0x9ff
	v_lshrrev_b32_e32 v40, 4, v236
	v_lshrrev_b32_e32 v2, 3, v236
	s_mov_b32 s10, s84
	s_cbranch_scc1 .LBB0_9
	v_and_b32_e32 v1, 15, v0
	v_lshlrev_b32_e32 v8, 4, v1
	v_lshlrev_b32_e32 v1, 3, v0
	v_mov_b32_e32 v9, 0
	v_lshrrev_b32_e32 v6, 3, v236
	v_and_b32_e32 v1, 56, v1
	s_waitcnt lgkmcnt(0)
	v_lshl_add_u64 v[4:5], s[4:5], 0, v[8:9]
	v_add_u32_e32 v3, s14, v8
	v_mul_u32_u24_e32 v7, 0x104, v40
	v_mul_u32_u24_e32 v10, 0x104, v1
	v_lshlrev_b32_e32 v8, 1, v1
	v_lshlrev_b32_e32 v1, 2, v6
	v_add3_u32 v1, s14, v10, v1
	v_add_u32_e32 v3, v3, v7
	v_lshl_add_u64 v[8:9], s[2:3], 0, v[8:9]
	v_or_b32_e32 v10, 8, v6
	v_or_b32_e32 v12, 16, v6
	v_or_b32_e32 v14, 24, v6
	v_or_b32_e32 v16, 32, v6
	v_or_b32_e32 v18, 40, v6
	v_or_b32_e32 v20, 48, v6
	v_or_b32_e32 v22, 56, v6
	s_lshl_b32 s0, s84, 6
	s_lshl_b32 s1, s66, 6
	s_movk_i32 s6, 0x50c0
	v_add_u32_e32 v7, 0x410, v3
	v_add_u32_e32 v11, 0x418, v3
	v_add_u32_e32 v13, 0x820, v3
	v_add_u32_e32 v15, 0x828, v3
	v_add_u32_e32 v17, 0xc30, v3
	v_add_u32_e32 v19, 0xc38, v3
	v_add_u32_e32 v21, 0x1040, v3
	v_add_u32_e32 v23, 0x1048, v3
	v_add_u32_e32 v41, 0x1450, v3
	v_add_u32_e32 v42, 0x1458, v3
	v_add_u32_e32 v43, 0x1860, v3
	v_add_u32_e32 v44, 0x1868, v3
	v_add_u32_e32 v45, 0x1c70, v3
	v_add_u32_e32 v46, 0x1c78, v3
	v_add_u32_e32 v47, 0x2080, v3
	v_add_u32_e32 v48, 0x2088, v3
	v_add_u32_e32 v49, 0x2490, v3
	v_add_u32_e32 v50, 0x2498, v3
	v_add_u32_e32 v51, 0x28a0, v3
	v_add_u32_e32 v52, 0x28a8, v3
	v_add_u32_e32 v53, 0x2cb0, v3
	v_add_u32_e32 v54, 0x2cb8, v3
	v_add_u32_e32 v55, 0x30c0, v3
	v_add_u32_e32 v56, 0x30c8, v3
	s_movk_i32 s7, 0x7fff
	s_mov_b32 s11, 0xffff0000
	v_add_u32_e32 v57, 0x34d0, v3
	v_add_u32_e32 v58, 0x34d8, v3
	v_add_u32_e32 v59, 0x38e0, v3
	v_add_u32_e32 v60, 0x38e8, v3
	v_add_u32_e32 v61, 0x3cf0, v3
	v_add_u32_e32 v62, 0x3cf8, v3
	v_add_u32_e32 v63, 0x400, v1
	s_mov_b32 s10, s84

.LBB0_159:
	v_readlane_b32 s30, v254, 1
	v_readlane_b32 s31, v254, 2
	s_mov_b32 s15, s99
	s_add_i32 s63, s63, 1
	s_mul_i32 s12, s63, s54
	s_waitcnt lgkmcnt(0)
	s_mul_hi_u32 s13, s63, s15
	s_add_i32 s13, s13, s12
	s_mul_i32 s12, s63, s15
	v_readlane_b32 s15, v254, 14
	s_add_u32 s30, s12, s15
	s_addc_u32 s31, s13, s55
	v_cmp_gt_i64_e32 vcc, s[30:31], v[178:179]
	v_cmp_lt_i64_e64 s[12:13], s[30:31], v[176:177]
	s_cbranch_vccnz .LBB0_161
	s_ashr_i32 s15, s30, 31
	s_lshr_b32 s15, s15, 29
	s_add_i32 s15, s30, s15
	s_ashr_i32 s26, s15, 3
	s_and_b32 s15, s15, -8
	s_sub_i32 s15, s30, s15
	s_cmp_lt_i32 s15, 0
	s_cselect_b32 s27, s56, 0x140
	s_mul_i32 s15, s15, s27
	s_add_i32 s15, s15, s26
	s_mul_hi_i32 s26, s15, 0x66666667
	s_lshr_b32 s27, s26, 31
	s_ashr_i32 s26, s26, 6
	s_add_i32 s26, s26, s27
	s_lshl_b32 s27, s26, 3
	s_sub_i32 s28, 0x80, s27
	s_min_i32 s28, s28, 8
	s_abs_i32 s29, s28
	v_cvt_f32_u32_e32 v2, s29
	s_sub_i32 s31, 0, s29
	s_mulk_i32 s26, 0xa0
	s_sub_i32 s15, s15, s26
	v_rcp_iflag_f32_e32 v2, v2
	s_abs_i32 s26, s15
	s_xor_b32 s30, s15, s28
	s_ashr_i32 s30, s30, 31
	v_mul_f32_e32 v2, 0x4f7ffffe, v2
	v_cvt_u32_f32_e32 v2, v2
	s_nop 0
	v_readfirstlane_b32 s34, v2
	s_mul_i32 s31, s31, s34
	s_mul_hi_u32 s31, s34, s31
	s_add_i32 s34, s34, s31
	s_mul_hi_u32 s31, s26, s34
	s_mul_i32 s34, s31, s29
	s_sub_i32 s26, s26, s34
	s_add_i32 s35, s31, 1
	s_sub_i32 s34, s26, s29
	s_cmp_ge_u32 s26, s29
	s_cselect_b32 s31, s35, s31
	s_cselect_b32 s26, s34, s26
	s_add_i32 s34, s31, 1
	s_cmp_ge_u32 s26, s29
	s_cselect_b32 s26, s34, s31
	s_xor_b32 s26, s26, s30
	s_sub_i32 s26, s26, s30
	s_mul_i32 s28, s26, s28
	s_sub_i32 s15, s15, s28
	s_add_i32 s28, s27, s15
.LBB0_161:
	s_ashr_i32 s29, s28, 31
	s_lshl_b64 s[30:31], s[28:29], 20
	v_readlane_b32 s34, v254, 18
	v_readlane_b32 s35, v254, 19
	s_add_u32 s30, s34, s30
	s_addc_u32 s31, s35, s31
	s_and_b64 s[34:35], s[12:13], exec
	s_cselect_b32 s15, s31, s17
	s_cselect_b32 s29, s30, s16
	s_ashr_i32 s27, s26, 31
	s_lshl_b64 s[34:35], s[26:27], 20
	s_add_u32 s34, s33, s34
	s_addc_u32 s35, s42, s35
	s_and_b64 s[38:39], s[12:13], exec
	s_cselect_b32 s27, s35, s37
	s_cselect_b32 s40, s34, s36
	s_add_u32 s16, s16, 0x80080
	s_addc_u32 s17, s17, 0
	s_add_u32 s41, s36, 0x100
	v_mov_b32_e32 v58, 0
	s_addc_u32 s64, s37, 0
	s_mov_b32 s65, -2
	v_mov_b32_e32 v59, 0
	v_mov_b64_e32 v[60:61], 0
	v_mov_b64_e32 v[62:63], 0
	v_mov_b64_e32 v[64:65], 0
	v_mov_b64_e32 v[74:75], 0
	v_mov_b64_e32 v[76:77], 0
	v_mov_b64_e32 v[78:79], 0
	v_mov_b64_e32 v[80:81], 0
	v_mov_b64_e32 v[82:83], 0
	v_mov_b64_e32 v[84:85], 0
	v_mov_b64_e32 v[86:87], 0
	v_mov_b64_e32 v[88:89], 0
	v_mov_b64_e32 v[106:107], 0
	v_mov_b64_e32 v[108:109], 0
	v_mov_b64_e32 v[110:111], 0
	v_mov_b64_e32 v[112:113], 0
	v_mov_b64_e32 v[2:3], 0
	v_mov_b64_e32 v[4:5], 0
	v_mov_b64_e32 v[6:7], 0
	v_mov_b64_e32 v[8:9], 0
	v_mov_b64_e32 v[10:11], 0
	v_mov_b64_e32 v[12:13], 0
	v_mov_b64_e32 v[14:15], 0
	v_mov_b64_e32 v[16:17], 0
	v_mov_b64_e32 v[18:19], 0
	v_mov_b64_e32 v[20:21], 0
	v_mov_b64_e32 v[22:23], 0
	v_mov_b64_e32 v[24:25], 0
	v_mov_b64_e32 v[26:27], 0
	v_mov_b64_e32 v[28:29], 0
	v_mov_b64_e32 v[30:31], 0
	v_mov_b64_e32 v[32:33], 0
	v_mov_b64_e32 v[114:115], 0
	v_mov_b64_e32 v[116:117], 0
	v_mov_b64_e32 v[118:119], 0
	v_mov_b64_e32 v[120:121], 0
	v_mov_b64_e32 v[122:123], 0
	v_mov_b64_e32 v[124:125], 0
	v_mov_b64_e32 v[126:127], 0
	v_mov_b64_e32 v[128:129], 0
	v_mov_b64_e32 v[130:131], 0
	v_mov_b64_e32 v[132:133], 0
	v_mov_b64_e32 v[134:135], 0
	v_mov_b64_e32 v[136:137], 0
	v_mov_b64_e32 v[138:139], 0
	v_mov_b64_e32 v[140:141], 0
	v_mov_b64_e32 v[142:143], 0
	v_mov_b64_e32 v[144:145], 0
	v_mov_b64_e32 v[34:35], 0
	v_mov_b64_e32 v[36:37], 0
	v_mov_b64_e32 v[38:39], 0
	v_mov_b64_e32 v[40:41], 0
	v_mov_b64_e32 v[42:43], 0
	v_mov_b64_e32 v[44:45], 0
	v_mov_b64_e32 v[46:47], 0
	v_mov_b64_e32 v[48:49], 0
	v_mov_b64_e32 v[50:51], 0
	v_mov_b64_e32 v[52:53], 0
	v_mov_b64_e32 v[54:55], 0
	v_mov_b64_e32 v[56:57], 0
	v_mov_b64_e32 v[66:67], 0
	v_mov_b64_e32 v[68:69], 0
	v_mov_b64_e32 v[70:71], 0
	v_mov_b64_e32 v[72:73], 0

.LBB0_421:
	s_mov_b64 s[30:31], s[8:9]
	v_readlane_b32 s8, v254, 1
	v_readlane_b32 s9, v254, 2
	s_mov_b32 s8, s99
	s_add_i32 s43, s43, 1
	s_mov_b64 s[0:1], s[10:11]
	s_mov_b32 s54, s36
	s_mov_b32 s53, s37
	s_waitcnt lgkmcnt(0)
	s_mul_i32 s10, s43, s8
	v_readlane_b32 s8, v254, 14
	s_add_i32 s10, s10, s8
	s_cmpk_lt_i32 s10, 0x100
	s_cselect_b64 s[34:35], -1, 0
	s_cmpk_gt_i32 s10, 0xff
	s_cselect_b64 s[28:29], -1, 0
	s_and_b64 vcc, exec, s[28:29]
	s_cbranch_vccnz .LBB0_427
	s_cmpk_gt_i32 s10, 0x7f
	s_mov_b64 s[8:9], -1
	s_cbranch_scc0 .LBB0_424
	s_add_i32 s36, s10, 0xffffff80
	s_add_i32 s24, s10, 0x158
	s_mov_b64 s[8:9], 0

.LBB0_427:
	s_ashr_i32 s25, s24, 31
	s_lshl_b64 s[8:9], s[24:25], 20
	s_add_u32 s10, s86, s8
	s_addc_u32 s11, s87, s9
	s_and_b64 s[8:9], s[34:35], exec
	s_cselect_b32 s25, s11, s1
	s_cselect_b32 s55, s10, s0
	s_ashr_i32 s27, s26, 31
	s_lshl_b64 s[8:9], s[26:27], 20
	s_add_u32 s8, s86, s8
	s_addc_u32 s9, s87, s9
	s_and_b64 s[34:35], s[34:35], exec
	s_cselect_b32 s27, s9, s31
	s_cselect_b32 s56, s8, s30
	s_add_u32 s0, s0, 0x80080
	s_addc_u32 s1, s1, 0
	s_add_u32 s57, s30, 0x100
	v_mov_b32_e32 v54, 0
	s_addc_u32 s58, s31, 0
	s_mov_b32 s59, -2
	v_mov_b32_e32 v55, 0
	v_mov_b64_e32 v[56:57], 0
	v_mov_b64_e32 v[58:59], 0
	v_mov_b64_e32 v[60:61], 0
	v_mov_b64_e32 v[62:63], 0
	v_mov_b64_e32 v[64:65], 0
	v_mov_b64_e32 v[70:71], 0
	v_mov_b64_e32 v[72:73], 0
	v_mov_b64_e32 v[74:75], 0
	v_mov_b64_e32 v[76:77], 0
	v_mov_b64_e32 v[78:79], 0
	v_mov_b64_e32 v[80:81], 0
	v_mov_b64_e32 v[82:83], 0
	v_mov_b64_e32 v[84:85], 0
	v_mov_b64_e32 v[90:91], 0
	v_mov_b64_e32 v[92:93], 0
	v_mov_b64_e32 v[2:3], 0
	v_mov_b64_e32 v[4:5], 0
	v_mov_b64_e32 v[6:7], 0
	v_mov_b64_e32 v[8:9], 0
	v_mov_b64_e32 v[10:11], 0
	v_mov_b64_e32 v[12:13], 0
	v_mov_b64_e32 v[14:15], 0
	v_mov_b64_e32 v[16:17], 0
	v_mov_b64_e32 v[18:19], 0
	v_mov_b64_e32 v[20:21], 0
	v_mov_b64_e32 v[22:23], 0
	v_mov_b64_e32 v[24:25], 0
	v_mov_b64_e32 v[26:27], 0
	v_mov_b64_e32 v[28:29], 0
	v_mov_b64_e32 v[30:31], 0
	v_mov_b64_e32 v[32:33], 0
	v_mov_b64_e32 v[98:99], 0
	v_mov_b64_e32 v[100:101], 0
	v_mov_b64_e32 v[102:103], 0
	v_mov_b64_e32 v[104:105], 0
	v_mov_b64_e32 v[106:107], 0
	v_mov_b64_e32 v[108:109], 0
	v_mov_b64_e32 v[110:111], 0
	v_mov_b64_e32 v[112:113], 0
	v_mov_b64_e32 v[114:115], 0
	v_mov_b64_e32 v[116:117], 0
	v_mov_b64_e32 v[118:119], 0
	v_mov_b64_e32 v[120:121], 0
	v_mov_b64_e32 v[122:123], 0
	v_mov_b64_e32 v[124:125], 0
	v_mov_b64_e32 v[126:127], 0
	v_mov_b64_e32 v[128:129], 0
	v_mov_b64_e32 v[34:35], 0
	v_mov_b64_e32 v[36:37], 0
	v_mov_b64_e32 v[38:39], 0
	v_mov_b64_e32 v[40:41], 0
	v_mov_b64_e32 v[42:43], 0
	v_mov_b64_e32 v[44:45], 0
	v_mov_b64_e32 v[46:47], 0
	v_mov_b64_e32 v[48:49], 0
	v_mov_b64_e32 v[50:51], 0
	v_mov_b64_e32 v[52:53], 0
	v_mov_b64_e32 v[66:67], 0
	v_mov_b64_e32 v[68:69], 0
	v_mov_b64_e32 v[86:87], 0
	v_mov_b64_e32 v[88:89], 0
	v_mov_b64_e32 v[94:95], 0
	v_mov_b64_e32 v[96:97], 0

.LBB0_1339:
	v_readlane_b32 s24, v254, 1
	v_readlane_b32 s25, v254, 2
	s_mov_b32 s21, s99
	s_add_i32 s44, s44, 1
	s_mul_i32 s8, s44, s47
	s_waitcnt lgkmcnt(0)
	s_mul_hi_u32 s9, s44, s21
	s_add_i32 s9, s9, s8
	s_mul_i32 s8, s44, s21
	v_readlane_b32 s21, v254, 14
	s_add_u32 s24, s8, s21
	s_addc_u32 s25, s9, s33
	v_cmp_gt_i64_e32 vcc, s[24:25], v[144:145]
	v_cmp_lt_i64_e64 s[8:9], s[24:25], v[142:143]
	s_cbranch_vccnz .LBB0_1345
	s_ashr_i32 s20, s24, 31
	s_lshr_b32 s20, s20, 29
	s_add_i32 s22, s24, s20
	s_and_b32 s20, s22, -8
	s_sub_i32 s23, s24, s20
	s_cmp_gt_i32 s23, -1
	s_mov_b64 s[20:21], -1
	s_cbranch_scc0 .LBB0_1342
	s_lshl_b32 s24, s23, 7
	s_mov_b64 s[20:21], 0

.LBB0_1345:
	s_ashr_i32 s23, s22, 31
	s_lshl_b64 s[24:25], s[22:23], 20
	v_readlane_b32 s26, v254, 22
	v_readlane_b32 s27, v254, 23
	s_add_u32 s24, s26, s24
	s_addc_u32 s25, s27, s25
	s_and_b64 s[26:27], s[8:9], exec
	s_cselect_b32 s23, s25, s31
	s_cselect_b32 s55, s24, s30
	s_ashr_i32 s21, s20, 31
	s_lshl_b64 s[26:27], s[20:21], 20
	s_add_u32 s26, s38, s26
	s_addc_u32 s27, s39, s27
	s_and_b64 s[36:37], s[8:9], exec
	s_cselect_b32 s21, s27, s35
	s_cselect_b32 s56, s26, s34
	s_add_u32 s30, s30, 0x80080
	s_addc_u32 s31, s31, 0
	s_add_u32 s57, s34, 0x100
	v_mov_b32_e32 v2, 0
	s_addc_u32 s58, s35, 0
	s_mov_b32 s59, -2
	v_mov_b32_e32 v3, 0
	v_mov_b64_e32 v[4:5], 0
	v_mov_b64_e32 v[6:7], 0
	v_mov_b64_e32 v[8:9], 0
	v_mov_b64_e32 v[10:11], 0
	v_mov_b64_e32 v[12:13], 0
	v_mov_b64_e32 v[18:19], 0
	v_mov_b64_e32 v[20:21], 0
	v_mov_b64_e32 v[26:27], 0
	v_mov_b64_e32 v[28:29], 0
	v_mov_b64_e32 v[34:35], 0
	v_mov_b64_e32 v[36:37], 0
	v_mov_b64_e32 v[42:43], 0
	v_mov_b64_e32 v[44:45], 0
	v_mov_b64_e32 v[50:51], 0
	v_mov_b64_e32 v[52:53], 0
	v_mov_b64_e32 v[14:15], 0
	v_mov_b64_e32 v[16:17], 0
	v_mov_b64_e32 v[22:23], 0
	v_mov_b64_e32 v[24:25], 0
	v_mov_b64_e32 v[30:31], 0
	v_mov_b64_e32 v[32:33], 0
	v_mov_b64_e32 v[38:39], 0
	v_mov_b64_e32 v[40:41], 0
	v_mov_b64_e32 v[46:47], 0
	v_mov_b64_e32 v[48:49], 0
	v_mov_b64_e32 v[54:55], 0
	v_mov_b64_e32 v[56:57], 0
	v_mov_b64_e32 v[58:59], 0
	v_mov_b64_e32 v[60:61], 0
	v_mov_b64_e32 v[62:63], 0
	v_mov_b64_e32 v[64:65], 0
	v_mov_b64_e32 v[66:67], 0
	v_mov_b64_e32 v[68:69], 0
	v_mov_b64_e32 v[70:71], 0
	v_mov_b64_e32 v[72:73], 0
	v_mov_b64_e32 v[74:75], 0
	v_mov_b64_e32 v[76:77], 0
	v_mov_b64_e32 v[82:83], 0
	v_mov_b64_e32 v[84:85], 0
	v_mov_b64_e32 v[90:91], 0
	v_mov_b64_e32 v[92:93], 0
	v_mov_b64_e32 v[98:99], 0
	v_mov_b64_e32 v[100:101], 0
	v_mov_b64_e32 v[106:107], 0
	v_mov_b64_e32 v[108:109], 0
	v_mov_b64_e32 v[114:115], 0
	v_mov_b64_e32 v[116:117], 0
	v_mov_b64_e32 v[78:79], 0
	v_mov_b64_e32 v[80:81], 0
	v_mov_b64_e32 v[86:87], 0
	v_mov_b64_e32 v[88:89], 0
	v_mov_b64_e32 v[94:95], 0
	v_mov_b64_e32 v[96:97], 0
	v_mov_b64_e32 v[102:103], 0
	v_mov_b64_e32 v[104:105], 0
	v_mov_b64_e32 v[110:111], 0
	v_mov_b64_e32 v[112:113], 0
	v_mov_b64_e32 v[118:119], 0
	v_mov_b64_e32 v[120:121], 0
	v_mov_b64_e32 v[122:123], 0
	v_mov_b64_e32 v[124:125], 0
	v_mov_b64_e32 v[126:127], 0
	v_mov_b64_e32 v[128:129], 0

.LBB0_1476:
	v_readlane_b32 s22, v254, 1
	v_readlane_b32 s23, v254, 2
	s_mov_b32 s17, s99
	s_add_i32 s43, s43, 1
	s_mul_i32 s8, s43, s46
	s_waitcnt lgkmcnt(0)
	s_mul_hi_u32 s9, s43, s17
	s_add_i32 s9, s9, s8
	s_mul_i32 s8, s43, s17
	v_readlane_b32 s17, v254, 14
	s_add_u32 s22, s8, s17
	s_addc_u32 s23, s9, s37
	v_cmp_gt_i64_e32 vcc, s[22:23], v[146:147]
	v_cmp_lt_i64_e64 s[8:9], s[22:23], v[144:145]
	s_cbranch_vccnz .LBB0_1478
	s_ashr_i32 s16, s22, 31
	s_lshr_b32 s16, s16, 29
	s_add_i32 s16, s22, s16
	s_ashr_i32 s17, s16, 3
	s_and_b32 s16, s16, -8
	s_sub_i32 s16, s22, s16
	s_cmp_lt_i32 s16, 0
	s_cselect_b32 s18, s38, 0x2c0
	s_mul_i32 s16, s16, s18
	s_add_i32 s16, s16, s17
	s_mul_hi_i32 s17, s16, 0x2e8ba2e9
	s_lshr_b32 s18, s17, 31
	s_ashr_i32 s17, s17, 6
	s_add_i32 s17, s17, s18
	s_lshl_b32 s18, s17, 3
	s_sub_i32 s19, 0x80, s18
	s_min_i32 s19, s19, 8
	s_abs_i32 s22, s19
	v_cvt_f32_u32_e32 v2, s22
	s_sub_i32 s24, 0, s22
	s_mulk_i32 s17, 0x160
	s_sub_i32 s17, s16, s17
	v_rcp_iflag_f32_e32 v2, v2
	s_abs_i32 s16, s17
	s_xor_b32 s23, s17, s19
	s_ashr_i32 s23, s23, 31
	v_mul_f32_e32 v2, 0x4f7ffffe, v2
	v_cvt_u32_f32_e32 v2, v2
	s_nop 0
	v_readfirstlane_b32 s25, v2
	s_mul_i32 s24, s24, s25
	s_mul_hi_u32 s24, s25, s24
	s_add_i32 s25, s25, s24
	s_mul_hi_u32 s24, s16, s25
	s_mul_i32 s25, s24, s22
	s_sub_i32 s16, s16, s25
	s_add_i32 s27, s24, 1
	s_sub_i32 s25, s16, s22
	s_cmp_ge_u32 s16, s22
	s_cselect_b32 s24, s27, s24
	s_cselect_b32 s16, s25, s16
	s_add_i32 s25, s24, 1
	s_cmp_ge_u32 s16, s22
	s_cselect_b32 s16, s25, s24
	s_xor_b32 s16, s16, s23
	s_sub_i32 s16, s16, s23
	s_mul_i32 s19, s16, s19
	s_sub_i32 s17, s17, s19
	s_add_i32 s18, s18, s17
.LBB0_1478:
	s_ashr_i32 s19, s18, 31
	s_lshl_b64 s[22:23], s[18:19], 20
	s_add_u32 s22, s20, s22
	s_addc_u32 s23, s21, s23
	s_and_b64 s[24:25], s[8:9], exec
	s_cselect_b32 s19, s23, s29
	s_cselect_b32 s27, s22, s28
	s_ashr_i32 s17, s16, 31
	s_lshl_b64 s[24:25], s[16:17], 20
	s_add_u32 s24, s15, s24
	s_addc_u32 s25, s33, s25
	s_and_b64 s[34:35], s[8:9], exec
	s_cselect_b32 s17, s25, s31
	s_cselect_b32 s51, s24, s30
	s_add_u32 s28, s28, 0x80080
	s_addc_u32 s29, s29, 0
	s_add_u32 s52, s30, 0x100
	v_mov_b32_e32 v2, 0
	s_addc_u32 s53, s31, 0
	s_mov_b32 s54, -2
	v_mov_b32_e32 v3, 0
	v_mov_b64_e32 v[4:5], 0
	v_mov_b64_e32 v[6:7], 0
	v_mov_b64_e32 v[8:9], 0
	v_mov_b64_e32 v[10:11], 0
	v_mov_b64_e32 v[12:13], 0
	v_mov_b64_e32 v[14:15], 0
	v_mov_b64_e32 v[16:17], 0
	v_mov_b64_e32 v[18:19], 0
	v_mov_b64_e32 v[20:21], 0
	v_mov_b64_e32 v[26:27], 0
	v_mov_b64_e32 v[28:29], 0
	v_mov_b64_e32 v[34:35], 0
	v_mov_b64_e32 v[36:37], 0
	v_mov_b64_e32 v[42:43], 0
	v_mov_b64_e32 v[44:45], 0
	v_mov_b64_e32 v[22:23], 0
	v_mov_b64_e32 v[24:25], 0
	v_mov_b64_e32 v[30:31], 0
	v_mov_b64_e32 v[32:33], 0
	v_mov_b64_e32 v[38:39], 0
	v_mov_b64_e32 v[40:41], 0
	v_mov_b64_e32 v[46:47], 0
	v_mov_b64_e32 v[48:49], 0
	v_mov_b64_e32 v[50:51], 0
	v_mov_b64_e32 v[52:53], 0
	v_mov_b64_e32 v[54:55], 0
	v_mov_b64_e32 v[56:57], 0
	v_mov_b64_e32 v[58:59], 0
	v_mov_b64_e32 v[60:61], 0
	v_mov_b64_e32 v[62:63], 0
	v_mov_b64_e32 v[64:65], 0
	v_mov_b64_e32 v[66:67], 0
	v_mov_b64_e32 v[68:69], 0
	v_mov_b64_e32 v[70:71], 0
	v_mov_b64_e32 v[72:73], 0
	v_mov_b64_e32 v[74:75], 0
	v_mov_b64_e32 v[76:77], 0
	v_mov_b64_e32 v[78:79], 0
	v_mov_b64_e32 v[80:81], 0
	v_mov_b64_e32 v[82:83], 0
	v_mov_b64_e32 v[84:85], 0
	s_waitcnt vmcnt(0)
	v_mov_b32_e32 v90, v2
	v_mov_b32_e32 v91, v2
	v_mov_b32_e32 v92, v2
	v_mov_b32_e32 v93, v2
	v_mov_b32_e32 v98, v2
	v_mov_b32_e32 v99, v2
	v_mov_b32_e32 v100, v2
	v_mov_b32_e32 v101, v2
	v_mov_b32_e32 v106, v2
	v_mov_b32_e32 v107, v2
	v_mov_b32_e32 v108, v2
	v_mov_b32_e32 v109, v2
	v_mov_b32_e32 v86, v2
	v_mov_b32_e32 v87, v2
	v_mov_b32_e32 v88, v2
	v_mov_b32_e32 v89, v2
	v_mov_b32_e32 v94, v2
	v_mov_b32_e32 v95, v2
	v_mov_b32_e32 v96, v2
	v_mov_b32_e32 v97, v2
	v_mov_b32_e32 v102, v2
	v_mov_b32_e32 v103, v2
	v_mov_b32_e32 v104, v2
	v_mov_b32_e32 v105, v2
	v_mov_b32_e32 v110, v2
	v_mov_b32_e32 v111, v2
	v_mov_b32_e32 v112, v2
	v_mov_b32_e32 v113, v2
	v_mov_b32_e32 v114, v2
	v_mov_b32_e32 v115, v2
	v_mov_b32_e32 v116, v2
	v_mov_b32_e32 v117, v2
	v_mov_b32_e32 v118, v2
	v_mov_b32_e32 v119, v2
	v_mov_b32_e32 v120, v2
	v_mov_b32_e32 v121, v2
	v_mov_b32_e32 v122, v2
	v_mov_b32_e32 v123, v2
	v_mov_b32_e32 v124, v2
	v_mov_b32_e32 v125, v2
	v_mov_b32_e32 v126, v2
	v_mov_b32_e32 v127, v2
	v_mov_b32_e32 v128, v2
	v_mov_b32_e32 v129, v2

.LBB0_1551:
	v_readlane_b32 s8, v254, 1
	v_readlane_b32 s9, v254, 2
	s_mov_b32 s8, s99
	s_add_i32 s43, s43, 1
	s_mul_i32 s0, s43, s46
	s_waitcnt lgkmcnt(0)
	s_mul_hi_u32 s1, s43, s8
	s_add_i32 s1, s1, s0
	s_mul_i32 s0, s43, s8
	v_readlane_b32 s8, v254, 14
	s_add_u32 s8, s0, s8
	s_addc_u32 s9, s1, s33
	v_cmp_gt_i64_e32 vcc, s[8:9], v[144:145]
	v_cmp_lt_i64_e64 s[0:1], s[8:9], v[142:143]
	s_cbranch_vccnz .LBB0_1557
	s_ashr_i32 s9, s8, 31
	s_lshr_b32 s9, s9, 29
	s_add_i32 s24, s8, s9
	s_and_b32 s9, s24, -8
	s_sub_i32 s25, s8, s9
	s_cmp_gt_i32 s25, -1
	s_mov_b64 s[8:9], -1
	s_cbranch_scc0 .LBB0_1554
	s_lshl_b32 s30, s25, 7
	s_mov_b64 s[8:9], 0

.LBB0_1561:
	s_add_u32 s26, s26, 0x160080
	s_addc_u32 s27, s27, 0
	s_add_u32 s57, s28, 0x100
	v_mov_b32_e32 v2, 0
	s_addc_u32 s58, s29, 0
	s_mov_b32 s59, -2
	v_mov_b32_e32 v3, 0
	v_mov_b64_e32 v[4:5], 0
	v_mov_b64_e32 v[6:7], 0
	v_mov_b64_e32 v[8:9], 0
	v_mov_b64_e32 v[10:11], 0
	v_mov_b64_e32 v[12:13], 0
	v_mov_b64_e32 v[18:19], 0
	v_mov_b64_e32 v[20:21], 0
	v_mov_b64_e32 v[26:27], 0
	v_mov_b64_e32 v[28:29], 0
	v_mov_b64_e32 v[34:35], 0
	v_mov_b64_e32 v[36:37], 0
	v_mov_b64_e32 v[42:43], 0
	v_mov_b64_e32 v[44:45], 0
	v_mov_b64_e32 v[50:51], 0
	v_mov_b64_e32 v[52:53], 0
	v_mov_b64_e32 v[14:15], 0
	v_mov_b64_e32 v[16:17], 0
	v_mov_b64_e32 v[22:23], 0
	v_mov_b64_e32 v[24:25], 0
	v_mov_b64_e32 v[30:31], 0
	v_mov_b64_e32 v[32:33], 0
	v_mov_b64_e32 v[38:39], 0
	v_mov_b64_e32 v[40:41], 0
	v_mov_b64_e32 v[46:47], 0
	v_mov_b64_e32 v[48:49], 0
	v_mov_b64_e32 v[54:55], 0
	v_mov_b64_e32 v[56:57], 0
	v_mov_b64_e32 v[58:59], 0
	v_mov_b64_e32 v[60:61], 0
	v_mov_b64_e32 v[62:63], 0
	v_mov_b64_e32 v[64:65], 0
	v_mov_b64_e32 v[66:67], 0
	v_mov_b64_e32 v[68:69], 0
	v_mov_b64_e32 v[70:71], 0
	v_mov_b64_e32 v[72:73], 0
	v_mov_b64_e32 v[74:75], 0
	v_mov_b64_e32 v[76:77], 0
	v_mov_b64_e32 v[82:83], 0
	v_mov_b64_e32 v[84:85], 0
	v_mov_b64_e32 v[90:91], 0
	v_mov_b64_e32 v[92:93], 0
	v_mov_b64_e32 v[98:99], 0
	v_mov_b64_e32 v[100:101], 0
	v_mov_b64_e32 v[106:107], 0
	v_mov_b64_e32 v[108:109], 0
	v_mov_b64_e32 v[114:115], 0
	v_mov_b64_e32 v[116:117], 0
	v_mov_b64_e32 v[78:79], 0
	v_mov_b64_e32 v[80:81], 0
	v_mov_b64_e32 v[86:87], 0
	v_mov_b64_e32 v[88:89], 0
	v_mov_b64_e32 v[94:95], 0
	v_mov_b64_e32 v[96:97], 0
	v_mov_b64_e32 v[102:103], 0
	v_mov_b64_e32 v[104:105], 0
	v_mov_b64_e32 v[110:111], 0
	v_mov_b64_e32 v[112:113], 0
	v_mov_b64_e32 v[118:119], 0
	v_mov_b64_e32 v[120:121], 0
	v_mov_b64_e32 v[122:123], 0
	v_mov_b64_e32 v[124:125], 0
	v_mov_b64_e32 v[126:127], 0
	v_mov_b64_e32 v[128:129], 0

.LBB0_1694:
	v_readlane_b32 s38, v254, 1
	v_readlane_b32 s39, v254, 2
	s_mov_b32 s35, s99
	s_add_i32 s57, s57, 1
	s_mul_i32 s10, s57, s63
	s_waitcnt lgkmcnt(0)
	s_mul_hi_u32 s11, s57, s35
	s_add_i32 s11, s11, s10
	s_mul_i32 s10, s57, s35
	v_readlane_b32 s35, v254, 14
	s_add_u32 s38, s10, s35
	s_addc_u32 s39, s11, s64
	v_cmp_gt_i64_e32 vcc, s[38:39], v[154:155]
	v_cmp_lt_i64_e64 s[10:11], s[38:39], v[152:153]
	s_cbranch_vccnz .LBB0_1696
	s_ashr_i32 s34, s38, 31
	s_lshr_b32 s34, s34, 29
	s_add_i32 s34, s38, s34
	s_ashr_i32 s35, s34, 3
	s_and_b32 s34, s34, -8
	s_sub_i32 s34, s38, s34
	s_cmp_lt_i32 s34, 0
	s_movk_i32 s36, 0x191
	s_cselect_b32 s36, s36, 0x190
	s_mul_i32 s34, s34, s36
	s_add_i32 s34, s34, s35
	s_mul_hi_i32 s35, s34, 0x51eb851f
	s_lshr_b32 s36, s35, 31
	s_ashr_i32 s35, s35, 6
	s_add_i32 s35, s35, s36
	s_lshl_b32 s36, s35, 3
	s_sub_i32 s37, 0x80, s36
	s_min_i32 s37, s37, 8
	s_abs_i32 s38, s37
	v_cvt_f32_u32_e32 v2, s38
	s_sub_i32 s40, 0, s38
	s_mulk_i32 s35, 0xc8
	s_sub_i32 s35, s34, s35
	v_rcp_iflag_f32_e32 v2, v2
	s_abs_i32 s34, s35
	s_xor_b32 s39, s35, s37
	s_ashr_i32 s39, s39, 31
	v_mul_f32_e32 v2, 0x4f7ffffe, v2
	v_cvt_u32_f32_e32 v2, v2
	s_nop 0
	v_readfirstlane_b32 s41, v2
	s_mul_i32 s40, s40, s41
	s_mul_hi_u32 s40, s41, s40
	s_add_i32 s41, s41, s40
	s_mul_hi_u32 s40, s34, s41
	s_mul_i32 s41, s40, s38
	s_sub_i32 s34, s34, s41
	s_add_i32 s43, s40, 1
	s_sub_i32 s41, s34, s38
	s_cmp_ge_u32 s34, s38
	s_cselect_b32 s40, s43, s40
	s_cselect_b32 s34, s41, s34
	s_add_i32 s41, s40, 1
	s_cmp_ge_u32 s34, s38
	s_cselect_b32 s34, s41, s40
	s_xor_b32 s34, s34, s39
	s_sub_i32 s34, s34, s39
	s_mul_i32 s37, s34, s37
	s_sub_i32 s35, s35, s37
	s_add_i32 s36, s36, s35
.LBB0_1696:
	s_ashr_i32 s37, s36, 31
	s_lshl_b64 s[38:39], s[36:37], 20
	s_add_u32 s38, s20, s38
	s_addc_u32 s39, s21, s39
	s_and_b64 s[40:41], s[10:11], exec
	s_cselect_b32 s37, s39, s47
	s_cselect_b32 s43, s38, s46
	s_ashr_i32 s35, s34, 31
	s_lshl_b64 s[40:41], s[34:35], 20
	s_add_u32 s40, s23, s40
	s_addc_u32 s41, s33, s41
	s_and_b64 s[50:51], s[10:11], exec
	s_cselect_b32 s35, s41, s49
	s_cselect_b32 s45, s40, s48
	s_add_u32 s46, s46, 0x80080
	s_addc_u32 s47, s47, 0
	s_add_u32 s69, s48, 0x100
	v_mov_b32_e32 v10, 0
	s_addc_u32 s70, s49, 0
	s_mov_b32 s71, -2
	v_mov_b32_e32 v11, v10
	v_mov_b32_e32 v12, v10
	v_mov_b32_e32 v13, v10
	v_mov_b32_e32 v30, v10
	v_mov_b32_e32 v31, v10
	v_mov_b32_e32 v32, v10
	v_mov_b32_e32 v33, v10
	v_mov_b32_e32 v22, v10
	v_mov_b32_e32 v23, v10
	v_mov_b32_e32 v24, v10
	v_mov_b32_e32 v25, v10
	v_mov_b32_e32 v26, v10
	v_mov_b32_e32 v27, v10
	v_mov_b32_e32 v28, v10
	v_mov_b32_e32 v29, v10
	v_mov_b32_e32 v14, v10
	v_mov_b32_e32 v15, v10
	v_mov_b32_e32 v16, v10
	v_mov_b32_e32 v17, v10
	v_mov_b32_e32 v18, v10
	v_mov_b32_e32 v19, v10
	v_mov_b32_e32 v20, v10
	v_mov_b32_e32 v21, v10
	v_mov_b32_e32 v2, v10
	v_mov_b32_e32 v3, v10
	v_mov_b32_e32 v4, v10
	v_mov_b32_e32 v5, v10
	v_mov_b32_e32 v6, v10
	v_mov_b32_e32 v7, v10
	v_mov_b32_e32 v8, v10
	v_mov_b32_e32 v9, v10
	v_mov_b32_e32 v66, v10
	v_mov_b32_e32 v67, v10
	v_mov_b32_e32 v68, v10
	v_mov_b32_e32 v69, v10
	v_mov_b32_e32 v70, v10
	v_mov_b32_e32 v71, v10
	v_mov_b32_e32 v72, v10
	v_mov_b32_e32 v73, v10
	v_mov_b32_e32 v74, v10
	v_mov_b32_e32 v75, v10
	v_mov_b32_e32 v76, v10
	v_mov_b32_e32 v77, v10
	v_mov_b32_e32 v78, v10
	v_mov_b32_e32 v79, v10
	v_mov_b32_e32 v80, v10
	v_mov_b32_e32 v81, v10
	v_mov_b32_e32 v82, v10
	v_mov_b32_e32 v83, v10
	v_mov_b32_e32 v84, v10
	v_mov_b32_e32 v85, v10
	v_mov_b32_e32 v86, v10
	v_mov_b32_e32 v87, v10
	v_mov_b32_e32 v88, v10
	v_mov_b32_e32 v89, v10
	s_waitcnt vmcnt(0)
	v_mov_b64_e32 v[90:91], 0
	v_mov_b64_e32 v[92:93], 0
	v_mov_b64_e32 v[94:95], 0
	v_mov_b64_e32 v[96:97], 0
	v_mov_b64_e32 v[58:59], 0
	v_mov_b64_e32 v[60:61], 0
	v_mov_b64_e32 v[62:63], 0
	v_mov_b64_e32 v[64:65], 0
	v_mov_b64_e32 v[50:51], 0
	v_mov_b64_e32 v[52:53], 0
	v_mov_b64_e32 v[54:55], 0
	v_mov_b64_e32 v[56:57], 0
	v_mov_b64_e32 v[42:43], 0
	v_mov_b64_e32 v[44:45], 0
	v_mov_b64_e32 v[46:47], 0
	v_mov_b64_e32 v[48:49], 0
	v_mov_b64_e32 v[34:35], 0
	v_mov_b64_e32 v[36:37], 0
	v_mov_b64_e32 v[38:39], 0
	v_mov_b64_e32 v[40:41], 0
	v_mov_b64_e32 v[98:99], 0
	v_mov_b64_e32 v[100:101], 0
	v_mov_b64_e32 v[102:103], 0
	v_mov_b64_e32 v[104:105], 0
	v_mov_b64_e32 v[106:107], 0
	v_mov_b64_e32 v[108:109], 0
	v_mov_b64_e32 v[110:111], 0
	v_mov_b64_e32 v[112:113], 0
	v_mov_b64_e32 v[114:115], 0
	v_mov_b64_e32 v[116:117], 0
	v_mov_b64_e32 v[118:119], 0
	v_mov_b64_e32 v[120:121], 0
	v_mov_b64_e32 v[122:123], 0
	v_mov_b64_e32 v[124:125], 0
	v_mov_b64_e32 v[126:127], 0
	v_mov_b64_e32 v[128:129], 0

.LBB0_2107:
	v_readlane_b32 s26, v254, 1
	v_readlane_b32 s27, v254, 2
	s_mov_b32 s23, s99
	s_add_i32 s46, s46, 1
	s_mul_i32 s4, s46, s49
	s_waitcnt lgkmcnt(0)
	s_mul_hi_u32 s5, s46, s23
	s_add_i32 s5, s5, s4
	s_mul_i32 s4, s46, s23
	v_readlane_b32 s23, v254, 14
	s_add_u32 s26, s4, s23
	s_addc_u32 s27, s5, s33
	v_cmp_gt_i64_e32 vcc, s[26:27], v[144:145]
	v_cmp_lt_i64_e64 s[4:5], s[26:27], v[142:143]
	s_cbranch_vccnz .LBB0_2113
	s_ashr_i32 s22, s26, 31
	s_lshr_b32 s22, s22, 29
	s_add_i32 s24, s26, s22
	s_and_b32 s22, s24, -8
	s_sub_i32 s25, s26, s22
	s_cmp_gt_i32 s25, -1
	s_mov_b64 s[22:23], -1
	s_cbranch_scc0 .LBB0_2110
	s_lshl_b32 s26, s25, 7
	s_mov_b64 s[22:23], 0

.LBB0_2113:
	s_ashr_i32 s25, s24, 31
	s_lshl_b64 s[26:27], s[24:25], 20
	v_readlane_b32 s28, v254, 22
	v_readlane_b32 s29, v254, 23
	s_add_u32 s26, s28, s26
	s_addc_u32 s27, s29, s27
	s_and_b64 s[28:29], s[4:5], exec
	s_cselect_b32 s25, s27, s35
	s_cselect_b32 s57, s26, s34
	s_ashr_i32 s23, s22, 31
	s_lshl_b64 s[28:29], s[22:23], 20
	s_add_u32 s28, s40, s28
	s_addc_u32 s29, s41, s29
	s_and_b64 s[38:39], s[4:5], exec
	s_cselect_b32 s23, s29, s37
	s_cselect_b32 s58, s28, s36
	s_add_u32 s34, s34, 0x80080
	s_addc_u32 s35, s35, 0
	s_add_u32 s59, s36, 0x100
	v_mov_b32_e32 v2, 0
	s_addc_u32 s60, s37, 0
	s_mov_b32 s61, -2
	v_mov_b32_e32 v3, 0
	v_mov_b64_e32 v[4:5], 0
	v_mov_b64_e32 v[6:7], 0
	v_mov_b64_e32 v[8:9], 0
	v_mov_b64_e32 v[10:11], 0
	v_mov_b64_e32 v[12:13], 0
	v_mov_b64_e32 v[18:19], 0
	v_mov_b64_e32 v[20:21], 0
	v_mov_b64_e32 v[26:27], 0
	v_mov_b64_e32 v[28:29], 0
	v_mov_b64_e32 v[34:35], 0
	v_mov_b64_e32 v[36:37], 0
	v_mov_b64_e32 v[42:43], 0
	v_mov_b64_e32 v[44:45], 0
	v_mov_b64_e32 v[50:51], 0
	v_mov_b64_e32 v[52:53], 0
	v_mov_b64_e32 v[14:15], 0
	v_mov_b64_e32 v[16:17], 0
	v_mov_b64_e32 v[22:23], 0
	v_mov_b64_e32 v[24:25], 0
	v_mov_b64_e32 v[30:31], 0
	v_mov_b64_e32 v[32:33], 0
	v_mov_b64_e32 v[38:39], 0
	v_mov_b64_e32 v[40:41], 0
	v_mov_b64_e32 v[46:47], 0
	v_mov_b64_e32 v[48:49], 0
	v_mov_b64_e32 v[54:55], 0
	v_mov_b64_e32 v[56:57], 0
	v_mov_b64_e32 v[58:59], 0
	v_mov_b64_e32 v[60:61], 0
	v_mov_b64_e32 v[62:63], 0
	v_mov_b64_e32 v[64:65], 0
	v_mov_b64_e32 v[66:67], 0
	v_mov_b64_e32 v[68:69], 0
	v_mov_b64_e32 v[70:71], 0
	v_mov_b64_e32 v[72:73], 0
	v_mov_b64_e32 v[74:75], 0
	v_mov_b64_e32 v[76:77], 0
	v_mov_b64_e32 v[82:83], 0
	v_mov_b64_e32 v[84:85], 0
	v_mov_b64_e32 v[90:91], 0
	v_mov_b64_e32 v[92:93], 0
	v_mov_b64_e32 v[98:99], 0
	v_mov_b64_e32 v[100:101], 0
	v_mov_b64_e32 v[106:107], 0
	v_mov_b64_e32 v[108:109], 0
	v_mov_b64_e32 v[114:115], 0
	v_mov_b64_e32 v[116:117], 0
	v_mov_b64_e32 v[78:79], 0
	v_mov_b64_e32 v[80:81], 0
	v_mov_b64_e32 v[86:87], 0
	v_mov_b64_e32 v[88:89], 0
	v_mov_b64_e32 v[94:95], 0
	v_mov_b64_e32 v[96:97], 0
	v_mov_b64_e32 v[102:103], 0
	v_mov_b64_e32 v[104:105], 0
	v_mov_b64_e32 v[110:111], 0
	v_mov_b64_e32 v[112:113], 0
	v_mov_b64_e32 v[118:119], 0
	v_mov_b64_e32 v[120:121], 0
	v_mov_b64_e32 v[122:123], 0
	v_mov_b64_e32 v[124:125], 0
	v_mov_b64_e32 v[126:127], 0
	v_mov_b64_e32 v[128:129], 0

.LBB0_2363:
	v_readlane_b32 s26, v254, 1
	v_readlane_b32 s27, v254, 2
	s_mov_b32 s23, s99
	s_add_i32 s7, s7, 1
	s_mul_i32 s4, s7, s59
	s_waitcnt lgkmcnt(0)
	s_mul_hi_u32 s5, s7, s23
	s_add_i32 s5, s5, s4
	s_mul_i32 s4, s7, s23
	v_readlane_b32 s23, v254, 14
	s_add_u32 s26, s4, s23
	s_addc_u32 s27, s5, s45
	v_cmp_ge_i64_e32 vcc, s[26:27], v[174:175]
	v_cmp_lt_i64_e64 s[4:5], s[26:27], v[174:175]
	s_cbranch_vccnz .LBB0_2365
	s_ashr_i32 s22, s26, 31
	s_lshr_b32 s22, s22, 29
	s_add_i32 s22, s26, s22
	s_ashr_i32 s23, s22, 3
	s_and_b32 s22, s22, -8
	s_sub_i32 s22, s26, s22
	s_cmp_lt_i32 s22, 0
	s_cselect_b32 s24, s46, s44
	s_mul_i32 s22, s24, s22
	s_add_i32 s22, s22, s23
	s_mul_hi_i32 s23, s22, 0x92492493
	s_add_i32 s23, s23, s22
	s_lshr_b32 s24, s23, 31
	s_ashr_i32 s23, s23, 8
	s_add_i32 s23, s23, s24
	s_lshl_b32 s24, s23, 3
	s_sub_i32 s25, s58, s24
	s_min_i32 s25, s25, 8
	s_abs_i32 s26, s25
	v_cvt_f32_u32_e32 v2, s26
	s_sub_i32 s28, 0, s26
	s_mulk_i32 s23, 0x1c0
	s_sub_i32 s22, s22, s23
	v_rcp_iflag_f32_e32 v2, v2
	s_abs_i32 s23, s22
	s_xor_b32 s27, s22, s25
	s_ashr_i32 s27, s27, 31
	v_mul_f32_e32 v2, 0x4f7ffffe, v2
	v_cvt_u32_f32_e32 v2, v2
	s_nop 0
	v_readfirstlane_b32 s29, v2
	s_mul_i32 s28, s28, s29
	s_mul_hi_u32 s28, s29, s28
	s_add_i32 s29, s29, s28
	s_mul_hi_u32 s28, s23, s29
	s_mul_i32 s29, s28, s26
	s_sub_i32 s23, s23, s29
	s_add_i32 s38, s28, 1
	s_sub_i32 s29, s23, s26
	s_cmp_ge_u32 s23, s26
	s_cselect_b32 s28, s38, s28
	s_cselect_b32 s23, s29, s23
	s_add_i32 s29, s28, 1
	s_cmp_ge_u32 s23, s26
	s_cselect_b32 s23, s29, s28
	s_xor_b32 s23, s23, s27
	s_sub_i32 s64, s23, s27
	s_mul_i32 s23, s64, s25
	s_sub_i32 s22, s22, s23
	s_add_i32 s22, s22, s24
	s_cmp_ge_i32 s22, s57
	s_cselect_b64 s[24:25], -1, 0
	s_cmp_ge_i32 s22, s33
	v_cndmask_b32_e64 v2, 0, 1, s[24:25]
	s_cselect_b64 s[24:25], -1, 0
	s_cmp_ge_i32 s22, s52
	v_cndmask_b32_e64 v3, 0, 1, s[24:25]
	s_cselect_b64 s[24:25], -1, 0
	v_readfirstlane_b32 s23, v3
	v_readfirstlane_b32 s26, v2
	s_cmp_lg_u64 s[24:25], 0
	s_addc_u32 s23, s23, s26
	s_cmp_ge_i32 s22, s53
	s_cselect_b64 s[24:25], -1, 0
	s_cmp_ge_i32 s22, s54
	v_cndmask_b32_e64 v2, 0, 1, s[24:25]
	s_cselect_b64 s[24:25], -1, 0
	v_readfirstlane_b32 s26, v2
	s_cmp_lg_u64 s[24:25], 0
	s_addc_u32 s23, s23, s26
	s_cmp_ge_i32 s22, s55
	s_cselect_b64 s[24:25], -1, 0
	s_cmp_ge_i32 s22, s56
	v_cndmask_b32_e64 v2, 0, 1, s[24:25]
	s_cselect_b64 s[24:25], -1, 0
	v_readfirstlane_b32 s26, v2
	s_cmp_lg_u64 s[24:25], 0
	s_addc_u32 s23, s23, s26
	s_mul_i32 s23, s23, 56
	s_add_i32 s24, s23, s64
.LBB0_2365:
	s_ashr_i32 s23, s22, 31
	s_lshl_b64 s[26:27], s[22:23], 19
	s_add_u32 s26, s19, s26
	s_addc_u32 s27, s40, s27
	s_and_b64 s[28:29], s[4:5], exec
	s_cselect_b32 s23, s27, s35
	s_cselect_b32 s66, s26, s34
	s_ashr_i32 s25, s24, 31
	s_lshl_b64 s[28:29], s[24:25], 19
	s_add_u32 s28, s41, s28
	s_addc_u32 s29, s42, s29
	s_and_b64 s[38:39], s[4:5], exec
	s_cselect_b32 s25, s29, s37
	s_cselect_b32 s67, s28, s36
	s_add_u32 s34, s34, 0x40080
	s_addc_u32 s35, s35, 0
	s_add_u32 s68, s36, 0x100
	v_mov_b32_e32 v34, 0
	s_addc_u32 s69, s37, 0
	s_mov_b32 s70, -2
	v_mov_b32_e32 v35, 0
	v_mov_b64_e32 v[36:37], 0
	v_mov_b64_e32 v[42:43], 0
	v_mov_b64_e32 v[44:45], 0
	v_mov_b64_e32 v[50:51], 0
	v_mov_b64_e32 v[52:53], 0
	v_mov_b64_e32 v[58:59], 0
	v_mov_b64_e32 v[60:61], 0
	v_mov_b64_e32 v[66:67], 0
	v_mov_b64_e32 v[68:69], 0
	v_mov_b64_e32 v[74:75], 0
	v_mov_b64_e32 v[76:77], 0
	v_mov_b64_e32 v[82:83], 0
	v_mov_b64_e32 v[84:85], 0
	v_mov_b64_e32 v[90:91], 0
	v_mov_b64_e32 v[92:93], 0
	v_mov_b64_e32 v[38:39], 0
	v_mov_b64_e32 v[40:41], 0
	v_mov_b64_e32 v[46:47], 0
	v_mov_b64_e32 v[48:49], 0
	v_mov_b64_e32 v[54:55], 0
	v_mov_b64_e32 v[56:57], 0
	v_mov_b64_e32 v[62:63], 0
	v_mov_b64_e32 v[64:65], 0
	v_mov_b64_e32 v[70:71], 0
	v_mov_b64_e32 v[72:73], 0
	v_mov_b64_e32 v[78:79], 0
	v_mov_b64_e32 v[80:81], 0
	v_mov_b64_e32 v[86:87], 0
	v_mov_b64_e32 v[88:89], 0
	v_mov_b64_e32 v[94:95], 0
	v_mov_b64_e32 v[96:97], 0
	v_mov_b64_e32 v[98:99], 0
	v_mov_b64_e32 v[100:101], 0
	v_mov_b64_e32 v[106:107], 0
	v_mov_b64_e32 v[108:109], 0
	v_mov_b64_e32 v[114:115], 0
	v_mov_b64_e32 v[116:117], 0
	v_mov_b64_e32 v[122:123], 0
	v_mov_b64_e32 v[124:125], 0
	v_mov_b64_e32 v[130:131], 0
	v_mov_b64_e32 v[132:133], 0
	v_mov_b64_e32 v[138:139], 0
	v_mov_b64_e32 v[140:141], 0
	v_mov_b64_e32 v[146:147], 0
	v_mov_b64_e32 v[148:149], 0
	v_mov_b64_e32 v[154:155], 0
	v_mov_b64_e32 v[156:157], 0
	v_mov_b64_e32 v[102:103], 0
	v_mov_b64_e32 v[104:105], 0
	v_mov_b64_e32 v[110:111], 0
	v_mov_b64_e32 v[112:113], 0
	v_mov_b64_e32 v[118:119], 0
	v_mov_b64_e32 v[120:121], 0
	v_mov_b64_e32 v[126:127], 0
	v_mov_b64_e32 v[128:129], 0
	v_mov_b64_e32 v[134:135], 0
	v_mov_b64_e32 v[136:137], 0
	v_mov_b64_e32 v[142:143], 0
	v_mov_b64_e32 v[144:145], 0
	v_mov_b64_e32 v[150:151], 0
	v_mov_b64_e32 v[152:153], 0
	v_mov_b64_e32 v[158:159], 0
	v_mov_b64_e32 v[160:161], 0

.LBB0_2434:
	v_readlane_b32 s4, v254, 1
	v_readlane_b32 s5, v254, 2
	s_mov_b32 s4, s99
	s_add_i32 s7, s7, 1
	s_mul_i32 s0, s7, s61
	s_waitcnt lgkmcnt(0)
	s_mul_hi_u32 s1, s7, s4
	s_add_i32 s1, s1, s0
	s_mul_i32 s0, s7, s4
	v_readlane_b32 s4, v254, 14
	s_add_u32 s4, s0, s4
	s_addc_u32 s5, s1, s45
	v_cmp_ge_i64_e32 vcc, s[4:5], v[172:173]
	v_cmp_lt_i64_e64 s[0:1], s[4:5], v[172:173]
	s_cbranch_vccnz .LBB0_2436
	s_ashr_i32 s5, s4, 31
	s_lshr_b32 s5, s5, 29
	s_add_i32 s5, s4, s5
	s_ashr_i32 s40, s5, 3
	s_and_b32 s5, s5, -8
	s_sub_i32 s4, s4, s5
	s_cmp_lt_i32 s4, 0
	s_cselect_b32 s5, s46, s58
	s_mul_i32 s4, s5, s4
	s_add_i32 s4, s4, s40
	s_ashr_i32 s5, s4, 31
	s_lshr_b32 s5, s5, 26
	s_add_i32 s5, s4, s5
	s_ashr_i32 s40, s5, 6
	s_lshl_b32 s40, s40, 3
	s_sub_i32 s41, s58, s40
	s_min_i32 s41, s41, 8
	s_abs_i32 s67, s41
	v_cvt_f32_u32_e32 v2, s67
	s_sub_i32 s71, 0, s67
	s_andn2_b32 s5, s5, 63
	s_sub_i32 s4, s4, s5
	v_rcp_iflag_f32_e32 v2, v2
	s_abs_i32 s5, s4
	s_xor_b32 s68, s4, s41
	s_ashr_i32 s68, s68, 31
	v_mul_f32_e32 v2, 0x4f7ffffe, v2
	v_cvt_u32_f32_e32 v2, v2
	s_nop 0
	v_readfirstlane_b32 s72, v2
	s_mul_i32 s71, s71, s72
	s_mul_hi_u32 s71, s72, s71
	s_add_i32 s72, s72, s71
	s_mul_hi_u32 s71, s5, s72
	s_mul_i32 s72, s71, s67
	s_sub_i32 s5, s5, s72
	s_add_i32 s73, s71, 1
	s_sub_i32 s72, s5, s67
	s_cmp_ge_u32 s5, s67
	s_cselect_b32 s71, s73, s71
	s_cselect_b32 s5, s72, s5
	s_add_i32 s72, s71, 1
	s_cmp_ge_u32 s5, s67
	s_cselect_b32 s5, s72, s71
	s_xor_b32 s5, s5, s68
	s_sub_i32 s67, s5, s68
	s_mul_i32 s5, s67, s41
	s_sub_i32 s4, s4, s5
	s_add_i32 s68, s4, s40
	s_cmp_ge_i32 s68, s57
	s_cselect_b64 s[4:5], -1, 0
	s_cmp_ge_i32 s68, s33
	v_cndmask_b32_e64 v2, 0, 1, s[4:5]
	s_cselect_b64 s[4:5], -1, 0
	s_cmp_ge_i32 s68, s52
	v_cndmask_b32_e64 v3, 0, 1, s[4:5]
	s_cselect_b64 vcc, -1, 0
	s_cmp_ge_i32 s68, s53
	v_addc_co_u32_e32 v2, vcc, v3, v2, vcc
	s_cselect_b64 s[4:5], -1, 0
	s_cmp_ge_i32 s68, s54
	v_cndmask_b32_e64 v3, 0, 1, s[4:5]
	s_cselect_b64 vcc, -1, 0
	s_cmp_ge_i32 s68, s55
	v_addc_co_u32_e32 v2, vcc, v2, v3, vcc
	s_cselect_b64 s[4:5], -1, 0
	s_cmp_ge_i32 s68, s56
	v_cndmask_b32_e64 v3, 0, 1, s[4:5]
	s_cselect_b64 vcc, -1, 0
	v_addc_co_u32_e32 v2, vcc, v2, v3, vcc
	v_lshlrev_b32_e32 v2, 3, v2
	v_add_u32_e32 v196, s67, v2

.LBB0_2440:
	s_add_u32 s38, s38, 0xe0080
	v_mov_b32_e32 v32, 0
	s_addc_u32 s39, s39, 0
	v_lshl_add_u64 v[176:177], v[0:1], 0, s[26:27]
	s_mov_b32 s71, -2
	v_mov_b32_e32 v33, 0
	v_mov_b64_e32 v[34:35], 0
	v_mov_b64_e32 v[36:37], 0
	v_mov_b64_e32 v[38:39], 0
	v_mov_b64_e32 v[40:41], 0
	v_mov_b64_e32 v[42:43], 0
	v_mov_b64_e32 v[48:49], 0
	v_mov_b64_e32 v[50:51], 0
	v_mov_b64_e32 v[56:57], 0
	v_mov_b64_e32 v[58:59], 0
	v_mov_b64_e32 v[64:65], 0
	v_mov_b64_e32 v[66:67], 0
	v_mov_b64_e32 v[72:73], 0
	v_mov_b64_e32 v[74:75], 0
	v_mov_b64_e32 v[80:81], 0
	v_mov_b64_e32 v[82:83], 0
	v_mov_b64_e32 v[44:45], 0
	v_mov_b64_e32 v[46:47], 0
	v_mov_b64_e32 v[52:53], 0
	v_mov_b64_e32 v[54:55], 0
	v_mov_b64_e32 v[60:61], 0
	v_mov_b64_e32 v[62:63], 0
	v_mov_b64_e32 v[68:69], 0
	v_mov_b64_e32 v[70:71], 0
	v_mov_b64_e32 v[76:77], 0
	v_mov_b64_e32 v[78:79], 0
	v_mov_b64_e32 v[84:85], 0
	v_mov_b64_e32 v[86:87], 0
	v_mov_b64_e32 v[88:89], 0
	v_mov_b64_e32 v[90:91], 0
	v_mov_b64_e32 v[92:93], 0
	v_mov_b64_e32 v[94:95], 0
	v_mov_b64_e32 v[96:97], 0
	v_mov_b64_e32 v[98:99], 0
	v_mov_b64_e32 v[100:101], 0
	v_mov_b64_e32 v[102:103], 0
	v_mov_b64_e32 v[104:105], 0
	v_mov_b64_e32 v[106:107], 0
	v_mov_b64_e32 v[112:113], 0
	v_mov_b64_e32 v[114:115], 0
	v_mov_b64_e32 v[120:121], 0
	v_mov_b64_e32 v[122:123], 0
	v_mov_b64_e32 v[128:129], 0
	v_mov_b64_e32 v[130:131], 0
	v_mov_b64_e32 v[136:137], 0
	v_mov_b64_e32 v[138:139], 0
	v_mov_b64_e32 v[144:145], 0
	v_mov_b64_e32 v[146:147], 0
	v_mov_b64_e32 v[108:109], 0
	v_mov_b64_e32 v[110:111], 0
	v_mov_b64_e32 v[116:117], 0
	v_mov_b64_e32 v[118:119], 0
	v_mov_b64_e32 v[124:125], 0
	v_mov_b64_e32 v[126:127], 0
	v_mov_b64_e32 v[132:133], 0
	v_mov_b64_e32 v[134:135], 0
	v_mov_b64_e32 v[140:141], 0
	v_mov_b64_e32 v[142:143], 0
	v_mov_b64_e32 v[148:149], 0
	v_mov_b64_e32 v[150:151], 0
	v_mov_b64_e32 v[152:153], 0
	v_mov_b64_e32 v[154:155], 0
	v_mov_b64_e32 v[156:157], 0
	v_mov_b64_e32 v[158:159], 0

	.amdhsa_kernel _Z6mk_fwd4Args
		.amdhsa_group_segment_fixed_size 0
		.amdhsa_private_segment_fixed_size 0
		.amdhsa_kernarg_size 440
		.amdhsa_user_sgpr_count 2
		.amdhsa_user_sgpr_dispatch_ptr 0
		.amdhsa_user_sgpr_queue_ptr 0
		.amdhsa_user_sgpr_kernarg_segment_ptr 1
		.amdhsa_user_sgpr_dispatch_id 0
		.amdhsa_user_sgpr_kernarg_preload_length 0
		.amdhsa_user_sgpr_kernarg_preload_offset 0
		.amdhsa_user_sgpr_private_segment_size 0
		.amdhsa_uses_dynamic_stack 0
		.amdhsa_enable_private_segment 0
		.amdhsa_system_sgpr_workgroup_id_x 1
		.amdhsa_system_sgpr_workgroup_id_y 0
		.amdhsa_system_sgpr_workgroup_id_z 0
		.amdhsa_system_sgpr_workgroup_info 0
		.amdhsa_system_vgpr_workitem_id 0
		.amdhsa_next_free_vgpr 256
		.amdhsa_next_free_sgpr 100
		.amdhsa_accum_offset 256
		.amdhsa_reserve_vcc 1
		.amdhsa_float_round_mode_32 0
		.amdhsa_float_round_mode_16_64 0
		.amdhsa_float_denorm_mode_32 3
		.amdhsa_float_denorm_mode_16_64 3
		.amdhsa_dx10_clamp 1
		.amdhsa_ieee_mode 1
		.amdhsa_fp16_overflow 0
		.amdhsa_tg_split 0
		.amdhsa_exception_fp_ieee_invalid_op 0
		.amdhsa_exception_fp_denorm_src 0
		.amdhsa_exception_fp_ieee_div_zero 0
		.amdhsa_exception_fp_ieee_overflow 0
		.amdhsa_exception_fp_ieee_underflow 0
		.amdhsa_exception_fp_ieee_inexact 0
		.amdhsa_exception_int_div_zero 0
	.end_amdhsa_kernel

amdhsa.kernels:
  - .agpr_count:     0
    .args:
      - .offset:         0
        .size:           184
        .value_kind:     by_value
      - .offset:         184
        .size:           4
        .value_kind:     hidden_block_count_x
      - .offset:         188
        .size:           4
        .value_kind:     hidden_block_count_y
      - .offset:         192
        .size:           4
        .value_kind:     hidden_block_count_z
      - .offset:         196
        .size:           2
        .value_kind:     hidden_group_size_x
      - .offset:         198
        .size:           2
        .value_kind:     hidden_group_size_y
      - .offset:         200
        .size:           2
        .value_kind:     hidden_group_size_z
      - .offset:         202
        .size:           2
        .value_kind:     hidden_remainder_x
      - .offset:         204
        .size:           2
        .value_kind:     hidden_remainder_y
      - .offset:         206
        .size:           2
        .value_kind:     hidden_remainder_z
      - .offset:         224
        .size:           8
        .value_kind:     hidden_global_offset_x
      - .offset:         232
        .size:           8
        .value_kind:     hidden_global_offset_y
      - .offset:         240
        .size:           8
        .value_kind:     hidden_global_offset_z
      - .offset:         248
        .size:           2
        .value_kind:     hidden_grid_dims
      - .offset:         304
        .size:           4
        .value_kind:     hidden_dynamic_lds_size
    .group_segment_fixed_size: 0
    .kernarg_segment_align: 8
    .kernarg_segment_size: 440
    .language:       OpenCL C
    .language_version:
      - 2
      - 0
    .max_flat_workgroup_size: 512
    .name:           _Z6mk_fwd4Args
    .private_segment_fixed_size: 0
    .sgpr_count:     106
    .sgpr_spill_count: 96
    .symbol:         _Z6mk_fwd4Args.kd
    .uniform_work_group_size: 1
    .uses_dynamic_stack: false
    .vgpr_count:     256
    .vgpr_spill_count: 0
    .wavefront_size: 64
